# MoE-up full rounds: each XCD owns a contiguous chunk of row tiles (4 per round) with all 8 column tiles, so consecutive rounds reuse an expert's weight tiles; last partial round unchanged
# baseline (speedup 1.0000x reference)
; __device__ __forceinline__ int otid() { int t = threadIdx.x; asm volatile("" : "+v"(t)); return t; }
;     __syncthreads();
;     const int tid = otid();
;     if (tid == 0) { int t = 0; for (int e = 0; e < 32; ++e) { tab[TAB_TPRE + e] = t; tab[TAB_OFFP + e] = t * 256; tab[TAB_CNT + e] = cnt[e]; t += (cnt[e] + 255) >> 8; } tab[TAB_TPRE + 32] = t; tab[TAB_OFFP + 32] = t * 256; }
;     __syncthreads();
;     if (ntn > 0 && tid < 32) {
;         const int total = tab[TAB_TPRE + 32] * ntn; int v = -1;
;         int Lx = tid * G + c;
;         if (ntn == 4 && G == 256) { const int x = c & 7, j = c >> 3; Lx = (tid * 64 + x * 8 + (j >> 2)) * 4 + (j & 3); }
;         if (Lx < total) { const int tile = Lx / ntn, pn = Lx % ntn; int e = 0; for (int k = 1; k < 32; ++k) e += (tab[TAB_TPRE + k] <= tile) ? 1 : 0; v = (e << 24) | ((tile - tab[TAB_TPRE + e]) << 8) | pn; }
;         tab[TAB_UNIT + tid] = v; tab[TAB_LX + tid] = Lx;
.LBB0_1661:
	s_or_b64 exec, exec, s[0:1]
	v_cmp_gt_i32_e32 vcc, 32, v1
	s_waitcnt lgkmcnt(0)
	s_barrier
	s_and_saveexec_b64 s[0:1], vcc
	s_cbranch_execz .LBB0_1665
	v_readlane_b32 s4, v254, 16
	s_nop 1
	v_mov_b32_e32 v2, s4
	ds_read_b32 v4, v2
	v_mul_lo_u32 v2, v1, s88
	s_bfe_u32 s72, s86, 0x20006
	s_lshl_b32 s72, s72, 3
	s_bfe_u32 s73, s86, 0x30003
	s_or_b32 s72, s72, s73
	s_and_b32 s73, s86, 7
	s_cmp_lg_u32 s88, 0x100
	s_cselect_b64 s[74:75], -1, 0
	s_waitcnt lgkmcnt(0)
	v_lshlrev_b32_e32 v4, 3, v4
	v_add_u32_e32 v5, 0x100, v2
	v_lshrrev_b32_e32 v6, 8, v4
	v_mul_u32_u24_e32 v6, s73, v6
	v_add_lshl_u32 v6, v6, v1, 5
	v_add_u32_e32 v6, s72, v6
	v_add_u32_e32 v7, s86, v2
	v_cmp_gt_i32_e32 vcc, v5, v4
	s_nop 1
	s_or_b64 vcc, vcc, s[74:75]
	s_nop 1
	v_cndmask_b32_e32 v2, v6, v7, vcc
	v_cmp_lt_i32_e32 vcc, v2, v4
	v_mov_b32_e32 v4, -1
	s_and_saveexec_b64 s[6:7], vcc
	s_cbranch_execz .LBB0_1664
	v_readlane_b32 s4, v254, 37
	v_ashrrev_i32_e32 v4, 31, v2
	v_lshrrev_b32_e32 v4, 29, v4
	v_mov_b32_e32 v6, s4
	ds_read2_b32 v[6:7], v6 offset1:1
	v_add_u32_e32 v5, v2, v4
	v_ashrrev_i32_e32 v4, 3, v5
	v_readlane_b32 s4, v254, 38
	v_and_b32_e32 v5, -8, v5
	s_waitcnt lgkmcnt(0)
	v_cmp_le_i32_e32 vcc, v6, v4
	v_mov_b32_e32 v6, s4
	v_readlane_b32 s4, v254, 39
	v_cndmask_b32_e64 v8, 0, 1, vcc
	v_cmp_le_i32_e32 vcc, v7, v4
	ds_read2_b32 v[6:7], v6 offset1:1
	v_sub_u32_e32 v5, v2, v5
	v_cndmask_b32_e64 v9, 0, 1, vcc
	s_waitcnt lgkmcnt(0)
	v_cmp_le_i32_e32 vcc, v6, v4
	s_nop 1
	v_addc_co_u32_e32 v8, vcc, v9, v8, vcc
	v_mov_b32_e32 v6, s4
	v_cmp_le_i32_e32 vcc, v7, v4
	ds_read2_b32 v[6:7], v6 offset1:1
	v_readlane_b32 s4, v254, 40
	v_cndmask_b32_e64 v9, 0, 1, vcc
	s_waitcnt lgkmcnt(0)
	v_cmp_le_i32_e32 vcc, v6, v4
	s_nop 1
	v_addc_co_u32_e32 v8, vcc, v8, v9, vcc
	v_mov_b32_e32 v6, s4
	v_cmp_le_i32_e32 vcc, v7, v4
	ds_read2_b32 v[6:7], v6 offset1:1
	v_readlane_b32 s4, v254, 41
	v_cndmask_b32_e64 v9, 0, 1, vcc
	s_waitcnt lgkmcnt(0)
	v_cmp_le_i32_e32 vcc, v6, v4
	s_nop 1
	v_addc_co_u32_e32 v8, vcc, v8, v9, vcc
	v_mov_b32_e32 v6, s4
	v_cmp_le_i32_e32 vcc, v7, v4
	ds_read2_b32 v[6:7], v6 offset1:1
	v_readlane_b32 s4, v254, 42
	v_cndmask_b32_e64 v9, 0, 1, vcc
	s_waitcnt lgkmcnt(0)
	v_cmp_le_i32_e32 vcc, v6, v4
	s_nop 1
	v_addc_co_u32_e32 v8, vcc, v8, v9, vcc
	v_mov_b32_e32 v6, s4
	v_cmp_le_i32_e32 vcc, v7, v4
	ds_read2_b32 v[6:7], v6 offset1:1
	v_readlane_b32 s4, v254, 43
	v_cndmask_b32_e64 v9, 0, 1, vcc
	s_waitcnt lgkmcnt(0)
	v_cmp_le_i32_e32 vcc, v6, v4
	s_nop 1
	v_addc_co_u32_e32 v8, vcc, v8, v9, vcc
	v_mov_b32_e32 v6, s4
	v_cmp_le_i32_e32 vcc, v7, v4
	ds_read2_b32 v[6:7], v6 offset1:1
	v_readlane_b32 s4, v254, 44
	v_cndmask_b32_e64 v9, 0, 1, vcc
	s_waitcnt lgkmcnt(0)
	v_cmp_le_i32_e32 vcc, v6, v4
	s_nop 1
	v_addc_co_u32_e32 v8, vcc, v8, v9, vcc
	v_mov_b32_e32 v6, s4
	v_cmp_le_i32_e32 vcc, v7, v4
	ds_read2_b32 v[6:7], v6 offset1:1
	v_readlane_b32 s4, v254, 45
	v_cndmask_b32_e64 v9, 0, 1, vcc
	s_waitcnt lgkmcnt(0)
	v_cmp_le_i32_e32 vcc, v6, v4
	s_nop 1
	v_addc_co_u32_e32 v8, vcc, v8, v9, vcc
	v_mov_b32_e32 v6, s4
	v_cmp_le_i32_e32 vcc, v7, v4
	ds_read2_b32 v[6:7], v6 offset1:1
	v_readlane_b32 s4, v254, 46
	v_cndmask_b32_e64 v9, 0, 1, vcc
	s_waitcnt lgkmcnt(0)
	v_cmp_le_i32_e32 vcc, v6, v4
	s_nop 1
	v_addc_co_u32_e32 v8, vcc, v8, v9, vcc
	v_mov_b32_e32 v6, s4
	v_cmp_le_i32_e32 vcc, v7, v4
	ds_read2_b32 v[6:7], v6 offset1:1
	v_readlane_b32 s4, v254, 47
	v_cndmask_b32_e64 v9, 0, 1, vcc
	s_waitcnt lgkmcnt(0)
	v_cmp_le_i32_e32 vcc, v6, v4
	s_nop 1
	v_addc_co_u32_e32 v8, vcc, v8, v9, vcc
	v_mov_b32_e32 v6, s4
	v_cmp_le_i32_e32 vcc, v7, v4
	ds_read2_b32 v[6:7], v6 offset1:1
	v_readlane_b32 s4, v254, 48
	v_cndmask_b32_e64 v9, 0, 1, vcc
	s_waitcnt lgkmcnt(0)
	v_cmp_le_i32_e32 vcc, v6, v4
	s_nop 1
	v_addc_co_u32_e32 v8, vcc, v8, v9, vcc
	v_mov_b32_e32 v6, s4
	v_cmp_le_i32_e32 vcc, v7, v4
	ds_read2_b32 v[6:7], v6 offset1:1
	v_readlane_b32 s4, v254, 49
	v_cndmask_b32_e64 v9, 0, 1, vcc
	s_waitcnt lgkmcnt(0)
	v_cmp_le_i32_e32 vcc, v6, v4
	s_nop 1
	v_addc_co_u32_e32 v8, vcc, v8, v9, vcc
	v_mov_b32_e32 v6, s4
	v_cmp_le_i32_e32 vcc, v7, v4
	ds_read2_b32 v[6:7], v6 offset1:1
	v_readlane_b32 s4, v254, 50
	v_cndmask_b32_e64 v9, 0, 1, vcc
	s_waitcnt lgkmcnt(0)
	v_cmp_le_i32_e32 vcc, v6, v4
	s_nop 1
	v_addc_co_u32_e32 v8, vcc, v8, v9, vcc
	v_mov_b32_e32 v6, s4
	v_cmp_le_i32_e32 vcc, v7, v4
	ds_read2_b32 v[6:7], v6 offset1:1
	v_readlane_b32 s4, v254, 51
	v_cndmask_b32_e64 v9, 0, 1, vcc
	s_waitcnt lgkmcnt(0)
	v_cmp_le_i32_e32 vcc, v6, v4
	s_nop 1
	v_addc_co_u32_e32 v8, vcc, v8, v9, vcc
	v_mov_b32_e32 v6, s4
	v_cmp_le_i32_e32 vcc, v7, v4
	ds_read2_b32 v[6:7], v6 offset1:1
	v_readlane_b32 s4, v254, 52
	v_cndmask_b32_e64 v9, 0, 1, vcc
	s_waitcnt lgkmcnt(0)
	v_cmp_le_i32_e32 vcc, v6, v4
	s_nop 1
	v_addc_co_u32_e32 v6, vcc, v8, v9, vcc
	v_mov_b32_e32 v8, s4
	ds_read_b32 v8, v8
	v_cmp_le_i32_e32 vcc, v7, v4
	s_nop 1
	v_cndmask_b32_e64 v7, 0, 1, vcc
	s_waitcnt lgkmcnt(0)
	v_cmp_le_i32_e32 vcc, v8, v4
	s_nop 1
	v_addc_co_u32_e32 v6, vcc, v6, v7, vcc
	v_lshlrev_b32_e32 v7, 24, v6
	v_lshl_add_u32 v6, v6, 2, 0
	v_add_u32_e32 v6, 0x20000, v6
	ds_read_b32 v6, v6
	s_waitcnt lgkmcnt(0)
	v_sub_u32_e32 v4, v4, v6
	v_lshlrev_b32_e32 v4, 8, v4
	v_or3_b32 v4, v4, v5, v7
